# v43 + loader waves at priority 2 during the GEMM phase
# baseline (speedup 1.0000x reference)
.LBB1_248:
	s_setprio 2
	v_and_b32_e32 v6, 31, v0
	v_bfe_u32 v7, v0, 5, 3
	s_cmp_lt_u32 s8, 0x2000
	s_cselect_b32 s50, s12, s14
	s_cselect_b32 s51, s13, s15
	s_and_b32 s0, s8, 0x1fff
	s_mul_i32 s1, s0, 0x2ee0
	s_add_u32 s50, s50, s1
	s_addc_u32 s51, s51, 0
	s_mov_b32 s52, s50
	s_mov_b32 s53, s51
	s_add_u32 s54, s50, 0x17700
	s_addc_u32 s55, s51, 0
	s_add_u32 s56, s50, 0x2ee00
	s_addc_u32 s57, s51, 0
	s_add_u32 s58, s50, 0x46500
	s_addc_u32 s59, s51, 0
	s_add_u32 s60, s50, 0x5dc00
	s_addc_u32 s61, s51, 0
	s_add_u32 s62, s50, 0x75300
	s_addc_u32 s63, s51, 0
	s_add_u32 s64, s50, 0x8ca00
	s_addc_u32 s65, s51, 0
	s_add_u32 s66, s50, 0xa4100
	s_addc_u32 s67, s51, 0
	v_and_b32_e32 v136, 3, v7
	v_lshl_add_u32 v137, v136, 1, v6
	s_movk_i32 s0, 0x2ee0
	v_mul_lo_u32 v2, v7, s0
	v_lshl_add_u32 v2, v137, 4, v2
	s_movk_i32 s0, 0x110
	v_mul_lo_u32 v3, v7, s0
	v_lshl_add_u32 v138, v137, 3, v3
	v_cmp_le_u32_e64 s[76:77], 32, v137
	v_cmp_gt_u32_e64 s[68:69], 14, v137
	s_not_b64 s[78:79], s[76:77]
	v_mov_b32_e32 v139, 0x0
	v_mov_b32_e32 v140, 0x4300
	v_cndmask_b32_e64 v139, v139, v140, s[76:77]
	v_add_u32_e32 v141, v138, v139
	v_mov_b32_e32 v139, 0x4400
	v_mov_b32_e32 v140, 0x8700
	v_cndmask_b32_e64 v139, v139, v140, s[76:77]
	v_add_u32_e32 v142, v138, v139
	v_mov_b32_e32 v139, 0x8800
	v_mov_b32_e32 v140, 0xcb00
	v_cndmask_b32_e64 v139, v139, v140, s[76:77]
	v_add_u32_e32 v143, v138, v139
	v_mov_b32_e32 v139, 0xcc00
	v_mov_b32_e32 v140, 0xffffff00
	v_cndmask_b32_e64 v139, v139, v140, s[76:77]
	v_add_u32_e32 v144, v138, v139
	s_add_u32 s48, s18, 0x100000
	s_addc_u32 s49, s19, 0
	s_lshl_b32 s0, s10, 12
	v_add_u32_e32 v150, 0xfffffe00, v0
	v_lshl_add_u32 v150, v150, 4, s0
	global_load_dwordx4 v[152:155], v150, s[48:49]
	global_load_dwordx4 v[156:159], v150, s[18:19]
	v_mov_b32_e32 v104, 0
	v_mov_b32_e32 v105, 0
	v_mov_b32_e32 v106, 0
	v_mov_b32_e32 v107, 0
	s_mov_b64 s[70:71], exec
	s_mov_b64 exec, s[76:77]
	global_load_dwordx4 v[104:107], v2, s[52:53] offset:-512 sc1 nt
	s_mov_b64 exec, s[70:71]
	v_mov_b32_e32 v108, 0
	v_mov_b32_e32 v109, 0
	v_mov_b32_e32 v110, 0
	v_mov_b32_e32 v111, 0
	s_mov_b64 s[70:71], exec
	s_mov_b64 exec, s[76:77]
	global_load_dwordx4 v[108:111], v2, s[54:55] offset:-512 sc1 nt
	s_mov_b64 exec, s[70:71]
	v_mov_b32_e32 v112, 0
	v_mov_b32_e32 v113, 0
	v_mov_b32_e32 v114, 0
	v_mov_b32_e32 v115, 0
	s_mov_b64 s[70:71], exec
	s_mov_b64 exec, s[76:77]
	global_load_dwordx4 v[112:115], v2, s[56:57] offset:-512 sc1 nt
	s_mov_b64 exec, s[70:71]
	v_mov_b32_e32 v116, 0
	v_mov_b32_e32 v117, 0
	v_mov_b32_e32 v118, 0
	v_mov_b32_e32 v119, 0
	s_mov_b64 s[70:71], exec
	s_mov_b64 exec, s[76:77]
	global_load_dwordx4 v[116:119], v2, s[58:59] offset:-512 sc1 nt
	s_mov_b64 exec, s[70:71]
	v_mov_b32_e32 v120, 0
	v_mov_b32_e32 v121, 0
	v_mov_b32_e32 v122, 0
	v_mov_b32_e32 v123, 0
	s_mov_b64 s[70:71], exec
	s_mov_b64 exec, s[76:77]
	global_load_dwordx4 v[120:123], v2, s[60:61] offset:-512 sc1 nt
	s_mov_b64 exec, s[70:71]
	v_mov_b32_e32 v124, 0
	v_mov_b32_e32 v125, 0
	v_mov_b32_e32 v126, 0
	v_mov_b32_e32 v127, 0
	s_mov_b64 s[70:71], exec
	s_mov_b64 exec, s[76:77]
	global_load_dwordx4 v[124:127], v2, s[62:63] offset:-512 sc1 nt
	s_mov_b64 exec, s[70:71]
	v_mov_b32_e32 v128, 0
	v_mov_b32_e32 v129, 0
	v_mov_b32_e32 v130, 0
	v_mov_b32_e32 v131, 0
	s_mov_b64 s[70:71], exec
	s_mov_b64 exec, s[76:77]
	global_load_dwordx4 v[128:131], v2, s[64:65] offset:-512 sc1 nt
	s_mov_b64 exec, s[70:71]
	v_mov_b32_e32 v132, 0
	v_mov_b32_e32 v133, 0
	v_mov_b32_e32 v134, 0
	v_mov_b32_e32 v135, 0
	s_mov_b64 s[70:71], exec
	s_mov_b64 exec, s[76:77]
	global_load_dwordx4 v[132:135], v2, s[66:67] offset:-512 sc1 nt
	s_mov_b64 exec, s[70:71]
	global_load_dwordx4 v[8:11], v2, s[52:53] sc1 nt
	global_load_dwordx4 v[12:15], v2, s[54:55] sc1 nt
	global_load_dwordx4 v[16:19], v2, s[56:57] sc1 nt
	global_load_dwordx4 v[20:23], v2, s[58:59] sc1 nt
	global_load_dwordx4 v[24:27], v2, s[60:61] sc1 nt
	global_load_dwordx4 v[28:31], v2, s[62:63] sc1 nt
	global_load_dwordx4 v[32:35], v2, s[64:65] sc1 nt
	global_load_dwordx4 v[36:39], v2, s[66:67] sc1 nt
	global_load_dwordx4 v[40:43], v2, s[52:53] offset:512 sc1 nt
	global_load_dwordx4 v[44:47], v2, s[54:55] offset:512 sc1 nt
	global_load_dwordx4 v[48:51], v2, s[56:57] offset:512 sc1 nt
	global_load_dwordx4 v[52:55], v2, s[58:59] offset:512 sc1 nt
	global_load_dwordx4 v[56:59], v2, s[60:61] offset:512 sc1 nt
	global_load_dwordx4 v[60:63], v2, s[62:63] offset:512 sc1 nt
	global_load_dwordx4 v[64:67], v2, s[64:65] offset:512 sc1 nt
	global_load_dwordx4 v[68:71], v2, s[66:67] offset:512 sc1 nt
	global_load_dwordx4 v[72:75], v2, s[52:53] offset:1024 sc1 nt
	global_load_dwordx4 v[76:79], v2, s[54:55] offset:1024 sc1 nt
	global_load_dwordx4 v[80:83], v2, s[56:57] offset:1024 sc1 nt
	global_load_dwordx4 v[84:87], v2, s[58:59] offset:1024 sc1 nt
	global_load_dwordx4 v[88:91], v2, s[60:61] offset:1024 sc1 nt
	global_load_dwordx4 v[92:95], v2, s[62:63] offset:1024 sc1 nt
	global_load_dwordx4 v[96:99], v2, s[64:65] offset:1024 sc1 nt
	global_load_dwordx4 v[100:103], v2, s[66:67] offset:1024 sc1 nt
	s_waitcnt vmcnt(31)
	v_cvt_pk_f16_f32 v4, v104, v105
	v_cvt_pk_f16_f32 v5, v106, v107
	s_mov_b64 s[70:71], exec
	s_mov_b64 exec, s[76:77]
	ds_write_b64 v144, v[4:5]
	s_mov_b64 exec, s[70:71]
	global_load_dwordx4 v[104:107], v2, s[52:53] offset:1536 sc1 nt
	s_waitcnt vmcnt(31)
	v_cvt_pk_f16_f32 v4, v108, v109
	v_cvt_pk_f16_f32 v5, v110, v111
	s_mov_b64 s[70:71], exec
	s_mov_b64 exec, s[76:77]
	ds_write_b64 v144, v[4:5] offset:2176
	s_mov_b64 exec, s[70:71]
	global_load_dwordx4 v[108:111], v2, s[54:55] offset:1536 sc1 nt
	s_waitcnt vmcnt(31)
	v_cvt_pk_f16_f32 v4, v112, v113
	v_cvt_pk_f16_f32 v5, v114, v115
	s_mov_b64 s[70:71], exec
	s_mov_b64 exec, s[76:77]
	ds_write_b64 v144, v[4:5] offset:4352
	s_mov_b64 exec, s[70:71]
	global_load_dwordx4 v[112:115], v2, s[56:57] offset:1536 sc1 nt
	s_waitcnt vmcnt(31)
	v_cvt_pk_f16_f32 v4, v116, v117
	v_cvt_pk_f16_f32 v5, v118, v119
	s_mov_b64 s[70:71], exec
	s_mov_b64 exec, s[76:77]
	ds_write_b64 v144, v[4:5] offset:6528
	s_mov_b64 exec, s[70:71]
	global_load_dwordx4 v[116:119], v2, s[58:59] offset:1536 sc1 nt
	s_waitcnt vmcnt(31)
	v_cvt_pk_f16_f32 v4, v120, v121
	v_cvt_pk_f16_f32 v5, v122, v123
	s_mov_b64 s[70:71], exec
	s_mov_b64 exec, s[76:77]
	ds_write_b64 v144, v[4:5] offset:8704
	s_mov_b64 exec, s[70:71]
	global_load_dwordx4 v[120:123], v2, s[60:61] offset:1536 sc1 nt
	s_waitcnt vmcnt(31)
	v_cvt_pk_f16_f32 v4, v124, v125
	v_cvt_pk_f16_f32 v5, v126, v127
	s_mov_b64 s[70:71], exec
	s_mov_b64 exec, s[76:77]
	ds_write_b64 v144, v[4:5] offset:10880
	s_mov_b64 exec, s[70:71]
	global_load_dwordx4 v[124:127], v2, s[62:63] offset:1536 sc1 nt
	s_waitcnt vmcnt(31)
	v_cvt_pk_f16_f32 v4, v128, v129
	v_cvt_pk_f16_f32 v5, v130, v131
	s_mov_b64 s[70:71], exec
	s_mov_b64 exec, s[76:77]
	ds_write_b64 v144, v[4:5] offset:13056
	s_mov_b64 exec, s[70:71]
	global_load_dwordx4 v[128:131], v2, s[64:65] offset:1536 sc1 nt
	s_waitcnt vmcnt(31)
	v_cvt_pk_f16_f32 v4, v132, v133
	v_cvt_pk_f16_f32 v5, v134, v135
	s_mov_b64 s[70:71], exec
	s_mov_b64 exec, s[76:77]
	ds_write_b64 v144, v[4:5] offset:15232
	s_mov_b64 exec, s[70:71]
	global_load_dwordx4 v[132:135], v2, s[66:67] offset:1536 sc1 nt
	s_waitcnt vmcnt(40)
	v_mov_b32_e32 v151, 1
	v_lshlrev_b32_e32 v160, 2, v152
	v_lshlrev_b32_e32 v161, 2, v153
	v_lshlrev_b32_e32 v162, 2, v154
	v_lshlrev_b32_e32 v163, 2, v155
	global_atomic_add v164, v160, v151, s[20:21] sc0
	global_atomic_add v165, v161, v151, s[20:21] sc0
	global_atomic_add v166, v162, v151, s[20:21] sc0
	global_atomic_add v167, v163, v151, s[20:21] sc0
	s_waitcnt vmcnt(35)
	v_cvt_pk_f16_f32 v4, v8, v9
	v_cvt_pk_f16_f32 v5, v10, v11
	ds_write_b64 v141, v[4:5]
	s_waitcnt vmcnt(27)
	v_cvt_pk_f16_f32 v4, v40, v41
	v_cvt_pk_f16_f32 v5, v42, v43
	ds_write_b64 v142, v[4:5]
	global_load_dwordx4 v[8:11], v2, s[52:53] offset:2048 sc1 nt
	global_load_dwordx4 v[40:43], v2, s[52:53] offset:2560 sc1 nt
	s_waitcnt vmcnt(36)
	v_cvt_pk_f16_f32 v4, v12, v13
	v_cvt_pk_f16_f32 v5, v14, v15
	ds_write_b64 v141, v[4:5] offset:2176
	s_waitcnt vmcnt(28)
	v_cvt_pk_f16_f32 v4, v44, v45
	v_cvt_pk_f16_f32 v5, v46, v47
	ds_write_b64 v142, v[4:5] offset:2176
	global_load_dwordx4 v[12:15], v2, s[54:55] offset:2048 sc1 nt
	global_load_dwordx4 v[44:47], v2, s[54:55] offset:2560 sc1 nt
	s_waitcnt vmcnt(37)
	v_cvt_pk_f16_f32 v4, v16, v17
	v_cvt_pk_f16_f32 v5, v18, v19
	ds_write_b64 v141, v[4:5] offset:4352
	s_waitcnt vmcnt(29)
	v_cvt_pk_f16_f32 v4, v48, v49
	v_cvt_pk_f16_f32 v5, v50, v51
	ds_write_b64 v142, v[4:5] offset:4352
	global_load_dwordx4 v[16:19], v2, s[56:57] offset:2048 sc1 nt
	global_load_dwordx4 v[48:51], v2, s[56:57] offset:2560 sc1 nt
	s_waitcnt vmcnt(38)
	v_cvt_pk_f16_f32 v4, v20, v21
	v_cvt_pk_f16_f32 v5, v22, v23
	ds_write_b64 v141, v[4:5] offset:6528
	s_waitcnt vmcnt(30)
	v_cvt_pk_f16_f32 v4, v52, v53
	v_cvt_pk_f16_f32 v5, v54, v55
	ds_write_b64 v142, v[4:5] offset:6528
	global_load_dwordx4 v[20:23], v2, s[58:59] offset:2048 sc1 nt
	global_load_dwordx4 v[52:55], v2, s[58:59] offset:2560 sc1 nt
	s_waitcnt vmcnt(39)
	v_cvt_pk_f16_f32 v4, v24, v25
	v_cvt_pk_f16_f32 v5, v26, v27
	ds_write_b64 v141, v[4:5] offset:8704
	s_waitcnt vmcnt(31)
	v_cvt_pk_f16_f32 v4, v56, v57
	v_cvt_pk_f16_f32 v5, v58, v59
	ds_write_b64 v142, v[4:5] offset:8704
	global_load_dwordx4 v[24:27], v2, s[60:61] offset:2048 sc1 nt
	global_load_dwordx4 v[56:59], v2, s[60:61] offset:2560 sc1 nt
	s_waitcnt vmcnt(40)
	v_cvt_pk_f16_f32 v4, v28, v29
	v_cvt_pk_f16_f32 v5, v30, v31
	ds_write_b64 v141, v[4:5] offset:10880
	s_waitcnt vmcnt(32)
	v_cvt_pk_f16_f32 v4, v60, v61
	v_cvt_pk_f16_f32 v5, v62, v63
	ds_write_b64 v142, v[4:5] offset:10880
	global_load_dwordx4 v[28:31], v2, s[62:63] offset:2048 sc1 nt
	global_load_dwordx4 v[60:63], v2, s[62:63] offset:2560 sc1 nt
	s_waitcnt vmcnt(41)
	v_cvt_pk_f16_f32 v4, v32, v33
	v_cvt_pk_f16_f32 v5, v34, v35
	ds_write_b64 v141, v[4:5] offset:13056
	s_waitcnt vmcnt(33)
	v_cvt_pk_f16_f32 v4, v64, v65
	v_cvt_pk_f16_f32 v5, v66, v67
	ds_write_b64 v142, v[4:5] offset:13056
	global_load_dwordx4 v[32:35], v2, s[64:65] offset:2048 sc1 nt
	global_load_dwordx4 v[64:67], v2, s[64:65] offset:2560 sc1 nt
	s_waitcnt vmcnt(42)
	v_cvt_pk_f16_f32 v4, v36, v37
	v_cvt_pk_f16_f32 v5, v38, v39
	ds_write_b64 v141, v[4:5] offset:15232
	s_waitcnt vmcnt(34)
	v_cvt_pk_f16_f32 v4, v68, v69
	v_cvt_pk_f16_f32 v5, v70, v71
	ds_write_b64 v142, v[4:5] offset:15232
	global_load_dwordx4 v[36:39], v2, s[66:67] offset:2048 sc1 nt
	global_load_dwordx4 v[68:71], v2, s[66:67] offset:2560 sc1 nt
	s_waitcnt vmcnt(0)
	v_cmp_gt_i32_e32 vcc, 64, v164
	v_lshl_add_u32 v148, v152, 6, v164
	v_lshlrev_b32_e32 v148, 2, v148
	s_and_saveexec_b64 s[2:3], vcc
	global_store_dword v148, v156, s[22:23]
	s_xor_b64 exec, exec, s[2:3]
	s_cbranch_execz .Lg1_ld_ok_0
	v_mov_b32_e32 v149, 0x8000
	global_atomic_add v149, v149, v151, s[20:21] sc0
	s_waitcnt vmcnt(0)
	v_lshlrev_b32_e32 v149, 3, v149
	v_mov_b32_e32 v160, v152
	v_mov_b32_e32 v161, v156
	global_store_dwordx2 v149, v[160:161], s[28:29]
